# gate/up queue: overflow positions mapped through a per-workgroup expert mask (no rejected positions), on top of the A-prefetch hoist
# baseline (speedup 1.0000x reference)
.LBB0_1279:
	s_cmp_le_i32 s74, s2
	s_cselect_b64 s[2:3], -1, 0
	s_and_b64 s[0:1], s[2:3], s[0:1]
	v_writelane_b32 v255, s0, 11
	s_andn2_b64 vcc, exec, s[0:1]
	s_nop 0
	v_writelane_b32 v255, s1, 12
	s_cbranch_vccnz .LBB0_1346
	v_readlane_b32 s0, v254, 41
	v_readlane_b32 s2, v254, 60
	v_readlane_b32 s3, v254, 61
	v_mov_b32_e32 v0, s0
	s_waitcnt vmcnt(0)
	ds_read_b64 v[2:3], v0
	s_mov_b32 s3, s57
	s_lshl_b32 s56, s2, 13
	s_lshl_b32 s0, s2, 8
	v_writelane_b32 v254, s2, 60
	s_waitcnt lgkmcnt(0)
	v_readfirstlane_b32 s15, v2
	s_lshl_b64 s[8:9], s[56:57], 2
	v_writelane_b32 v254, s3, 61
	s_lshl_b64 s[2:3], s[2:3], 28
	v_readfirstlane_b32 s16, v3
	s_add_u32 s8, s15, s8
	v_readlane_b32 s11, v253, 0
	s_addc_u32 s9, s16, s9
	v_mbcnt_lo_u32_b32 v0, -1, 0
	v_mbcnt_hi_u32_b32 v0, -1, v0
	s_mov_b32 s1, s57
	v_add_u32_e32 v231, s11, v0
	s_add_u32 s50, s8, 0x10000
	v_readfirstlane_b32 s8, v231
	s_addc_u32 s51, s9, 0
	s_ashr_i32 s9, s8, 6
	s_lshl_b64 s[18:19], s[0:1], 2
	s_add_u32 s0, s15, s18
	v_writelane_b32 v255, s18, 13
	s_addc_u32 s1, s16, s19
	s_add_u32 s52, s0, 0xa000
	s_addc_u32 s53, s1, 0
	v_readlane_b32 s11, v254, 53
	v_writelane_b32 v255, s19, 14
	s_add_u32 s0, s15, 0x2e3e0000
	v_mov_b32_e32 v0, s11
	v_writelane_b32 v255, s0, 15
	s_addc_u32 s0, s16, 0
	ds_read_b128 v[2:5], v0
	s_add_u32 s54, s15, 0x4ffe0a00
	s_addc_u32 s55, s16, 0
	s_add_u32 s58, s15, 0x2f3e0000
	v_writelane_b32 v255, s0, 16
	s_addc_u32 s59, s16, 0
	s_ashr_i32 s0, s8, 7
	s_and_b32 s1, s9, 1
	v_writelane_b32 v255, s15, 17
	s_lshl_b32 s28, s0, 5
	s_lshl_b32 s15, s1, 5
	s_waitcnt lgkmcnt(0)
	v_readfirstlane_b32 s11, v2
	v_readfirstlane_b32 s13, v4
	s_cmp_lt_i32 s0, 2
	v_readfirstlane_b32 s12, v3
	v_readfirstlane_b32 s14, v5
	s_cselect_b32 s11, s11, s13
	s_cselect_b32 s0, s12, s14
	s_add_u32 s2, s11, s2
	v_writelane_b32 v255, s16, 18
	s_addc_u32 s0, s0, s3
	s_lshl_b32 s3, s9, 8
	v_writelane_b32 v255, s15, 5
	s_add_i32 s3, s3, 0
	v_writelane_b32 v255, s3, 7
	s_and_b32 s3, s8, 0x80
	s_add_u32 s2, s2, s3
	s_addc_u32 s0, s0, 0
	s_and_b32 s83, s8, 0xffffffc0
	v_writelane_b32 v255, s2, 19
	s_lshl_b32 s2, s83, 2
	s_add_i32 s87, s2, 0
	s_ashr_i32 s2, s8, 8
	v_writelane_b32 v255, s0, 20
	s_lshl_b32 s0, s9, 5
	s_lshl_b32 s3, s2, 13
	s_and_b32 s0, s0, 0xffffff80
	s_add_i32 s3, s3, 0
	s_lshl_b32 s1, s1, 12
	s_add_i32 s0, s0, 0
	s_add_i32 s78, s3, s1
	v_writelane_b32 v255, s0, 9
	s_and_b32 s0, s9, 3
	s_or_b32 s80, s83, 32
	s_add_i32 s78, s78, 0x10000
	s_cmp_gt_u32 s0, 1
	s_cselect_b64 s[60:61], -1, 0
	s_cmp_lt_u32 s0, 2
	s_mul_i32 s33, s0, 0x1200
	s_cselect_b64 s[62:63], -1, 0
	s_lshl_b32 s64, s0, 5
	s_lshl_b32 s0, s9, 4
	s_and_b32 s0, s0, 16
	v_cmp_eq_u32_e64 s[18:19], 0, v231
	v_writelane_b32 v255, s0, 3
	s_lshl_b32 s1, s2, 7
	v_writelane_b32 v255, s18, 21
	s_add_i32 s3, s1, 0
	s_mov_b32 s65, s57
	v_writelane_b32 v255, s19, 22
	s_mov_b64 s[46:47], exec
	s_mov_b64 exec, -1
	v_and_b32_e32 v5, 63, v231
	v_lshlrev_b32_e32 v5, 7, v5
	v_add_u32_e32 v6, 0x2000, v5
	v_add_u32_e32 v7, 0x4000, v5
	v_add_u32_e32 v8, 0x6000, v5
	global_load_dword v9, v5, s[50:51]
	global_load_dword v10, v6, s[50:51]
	global_load_dword v11, v7, s[50:51]
	global_load_dword v12, v8, s[50:51]
	s_movk_i32 s36, 0x240
	s_waitcnt vmcnt(3)
	v_cmp_lt_i32_e64 s[38:39], s36, v9
	s_waitcnt vmcnt(2)
	v_cmp_lt_i32_e64 s[40:41], s36, v10
	s_waitcnt vmcnt(1)
	v_cmp_lt_i32_e64 s[42:43], s36, v11
	s_waitcnt vmcnt(0)
	v_cmp_lt_i32_e64 s[44:45], s36, v12
	s_nop 3
	v_writelane_b32 v252, s38, 0
	v_writelane_b32 v252, s39, 1
	v_writelane_b32 v252, s40, 2
	v_writelane_b32 v252, s41, 3
	v_writelane_b32 v252, s42, 4
	v_writelane_b32 v252, s43, 5
	v_writelane_b32 v252, s44, 6
	v_writelane_b32 v252, s45, 7
	s_bcnt1_i32_b64 s36, s[38:39]
	s_bcnt1_i32_b64 s37, s[40:41]
	s_add_i32 s36, s36, s37
	s_bcnt1_i32_b64 s37, s[42:43]
	s_add_i32 s36, s36, s37
	s_bcnt1_i32_b64 s37, s[44:45]
	s_add_i32 s36, s36, s37
	s_nop 0
	v_writelane_b32 v252, s36, 8
	s_mov_b64 exec, s[46:47]
	s_branch .LBB0_1283

.LBB0_1288:
	s_or_b64 exec, exec, s[12:13]
	s_waitcnt vmcnt(0)
	v_readfirstlane_b32 s2, v2
	s_mov_b64 s[14:15], -1
	s_nop 0
	v_add_u32_e32 v2, s2, v0
	v_add_u32_e32 v0, 0xffffff00, v2
	s_movk_i32 s2, 0x400
	v_cmp_gt_u32_e32 vcc, s2, v0
	s_and_saveexec_b64 s[12:13], vcc
	s_cbranch_execz .LBB0_1285
	v_readfirstlane_b32 s36, v0
	v_readlane_b32 s37, v252, 8
	s_lshr_b32 s38, s36, 2
	s_and_b32 s36, s36, 3
	s_movk_i32 s39, 0x500
	s_cmp_ge_u32 s38, s37
	s_cbranch_scc1 .Lgq_set
	s_mov_b32 s40, 0
	v_readlane_b32 s42, v252, 0
	v_readlane_b32 s43, v252, 1
	s_bcnt1_i32_b64 s41, s[42:43]
	s_cmp_lt_u32 s38, s41
	s_cbranch_scc1 .Lgq_word
	s_sub_i32 s38, s38, s41
	s_movk_i32 s40, 64
	v_readlane_b32 s42, v252, 2
	v_readlane_b32 s43, v252, 3
	s_bcnt1_i32_b64 s41, s[42:43]
	s_cmp_lt_u32 s38, s41
	s_cbranch_scc1 .Lgq_word
	s_sub_i32 s38, s38, s41
	s_movk_i32 s40, 128
	v_readlane_b32 s42, v252, 4
	v_readlane_b32 s43, v252, 5
	s_bcnt1_i32_b64 s41, s[42:43]
	s_cmp_lt_u32 s38, s41
	s_cbranch_scc1 .Lgq_word
	s_sub_i32 s38, s38, s41
	s_movk_i32 s40, 192
	v_readlane_b32 s42, v252, 6
	v_readlane_b32 s43, v252, 7
.Lgq_word:
	s_cmp_eq_u32 s38, 0
	s_cbranch_scc1 .Lgq_bit
	s_ff1_i32_b64 s41, s[42:43]
	s_bitset0_b64 s[42:43], s41
	s_sub_i32 s38, s38, 1
	s_branch .Lgq_word
.Lgq_bit:
	s_ff1_i32_b64 s41, s[42:43]
	s_add_i32 s40, s40, s41
	s_lshl_b32 s40, s40, 2
	s_add_i32 s40, s40, s36
	s_add_i32 s39, s40, 0x100
.Lgq_set:
	v_mov_b32_e32 v2, s39
	s_branch .LBB0_1285
